# v66 + in-projection and gates epilogues no longer drain the chained next-tile loads before they start (hipcc artifact wait vmcnt(0) -> vmcnt(8))
# speedup vs baseline: 1.0116x; 1.0116x over previous
.LBB0_1061:
	s_waitcnt vmcnt(8)
	v_ffbh_u32_e32 v159, v157
	v_min_u32_e32 v159, 32, v159
	v_lshlrev_b64 v[156:157], v159, v[156:157]
	v_min_u32_e32 v156, 1, v156
	v_or_b32_e32 v156, v157, v156
	v_cvt_f32_u32_e32 v156, v156
	v_sub_u32_e32 v157, 32, v159
	s_mov_b32 s36, 0x358637bd
	v_mov_b64_e32 v[164:165], s[36:37]
	v_ldexp_f32 v157, v156, v157
	v_ffbh_u32_e32 v156, v155
	v_min_u32_e32 v156, 32, v156
	v_lshlrev_b64 v[154:155], v156, v[154:155]
	v_min_u32_e32 v154, 1, v154
	v_or_b32_e32 v154, v155, v154
	v_cvt_f32_u32_e32 v154, v154
	v_sub_u32_e32 v155, 32, v156
	s_mov_b32 s48, 0x32800000
	s_mov_b32 s29, -1
	v_ldexp_f32 v156, v154, v155
	v_pk_fma_f32 v[154:155], v[156:157], s[48:49], v[164:165] op_sel_hi:[1,0,0]
	v_readlane_b32 s92, v253, 28
	v_mul_f32_e32 v156, 0x4b800000, v155
	v_cmp_gt_f32_e64 s[36:37], s96, v155
	v_cmp_gt_f32_e32 vcc, s96, v154
	v_mbcnt_lo_u32_b32 v0, s29, 0
	v_cndmask_b32_e64 v155, v155, v156, s[36:37]
	v_rsq_f32_e32 v155, v155
	v_mbcnt_hi_u32_b32 v0, s29, v0
	s_lshl_b32 s29, s84, 8
	s_add_i32 s29, s29, s52
	v_mul_f32_e32 v156, 0x45800000, v155
	v_cndmask_b32_e64 v155, v155, v156, s[36:37]
	v_mul_f32_e32 v156, 0x4b800000, v154
	v_cndmask_b32_e32 v154, v154, v156, vcc
	v_rsq_f32_e32 v154, v154
	v_and_or_b32 v158, v0, 15, s29
	v_and_b32_e32 v0, 0x70, v0
	v_ashrrev_i32_e32 v159, 31, v158
	v_mul_f32_e32 v156, 0x45800000, v154
	v_cndmask_b32_e32 v154, v154, v156, vcc
	v_ffbh_u32_e32 v156, v153
	v_min_u32_e32 v156, 32, v156
	v_lshlrev_b64 v[152:153], v156, v[152:153]
	v_min_u32_e32 v152, 1, v152
	v_or_b32_e32 v152, v153, v152
	v_cvt_f32_u32_e32 v152, v152
	v_sub_u32_e32 v153, 32, v156
	s_mov_b32 s89, 0x2e8ba2e9
	s_movk_i32 s90, 0xfea0
	v_ldexp_f32 v153, v152, v153
	v_ffbh_u32_e32 v152, v151
	v_min_u32_e32 v152, 32, v152
	v_lshlrev_b64 v[150:151], v152, v[150:151]
	v_min_u32_e32 v150, 1, v150
	v_or_b32_e32 v150, v151, v150
	v_cvt_f32_u32_e32 v150, v150
	v_sub_u32_e32 v151, 32, v152
	v_readlane_b32 s93, v253, 29
	v_ldexp_f32 v152, v150, v151
	v_pk_fma_f32 v[150:151], v[152:153], s[48:49], v[164:165] op_sel_hi:[1,0,0]
	s_nop 0
	v_mul_f32_e32 v152, 0x4b800000, v151
	v_cmp_gt_f32_e64 s[36:37], s96, v151
	v_cmp_gt_f32_e32 vcc, s96, v150
	s_nop 0
	v_cndmask_b32_e64 v151, v151, v152, s[36:37]
	v_rsq_f32_e32 v151, v151
	s_nop 0
	v_mul_f32_e32 v152, 0x45800000, v151
	v_cndmask_b32_e64 v151, v151, v152, s[36:37]
	v_mul_f32_e32 v152, 0x4b800000, v150
	v_cndmask_b32_e32 v150, v150, v152, vcc
	v_rsq_f32_e32 v150, v150
	s_nop 0
	v_mul_f32_e32 v152, 0x45800000, v150
	v_cndmask_b32_e32 v150, v150, v152, vcc
	v_ffbh_u32_e32 v152, v149
	v_min_u32_e32 v152, 32, v152
	v_lshlrev_b64 v[148:149], v152, v[148:149]
	v_min_u32_e32 v148, 1, v148
	v_or_b32_e32 v148, v149, v148
	v_cvt_f32_u32_e32 v148, v148
	v_sub_u32_e32 v149, 32, v152
	v_ldexp_f32 v149, v148, v149
	v_ffbh_u32_e32 v148, v147
	v_min_u32_e32 v148, 32, v148
	v_lshlrev_b64 v[146:147], v148, v[146:147]
	v_min_u32_e32 v146, 1, v146
	v_or_b32_e32 v146, v147, v146
	v_cvt_f32_u32_e32 v146, v146
	v_sub_u32_e32 v147, 32, v148
	v_ldexp_f32 v148, v146, v147
	v_pk_fma_f32 v[146:147], v[148:149], s[48:49], v[164:165] op_sel_hi:[1,0,0]
	s_nop 0
	v_mul_f32_e32 v148, 0x4b800000, v147
	v_cmp_gt_f32_e64 s[36:37], s96, v147
	v_cmp_gt_f32_e32 vcc, s96, v146
	s_nop 0
	v_cndmask_b32_e64 v147, v147, v148, s[36:37]
	v_rsq_f32_e32 v147, v147
	s_nop 0
	v_mul_f32_e32 v148, 0x45800000, v147
	v_cndmask_b32_e64 v149, v147, v148, s[36:37]
	v_mul_f32_e32 v147, 0x4b800000, v146
	v_cndmask_b32_e32 v146, v146, v147, vcc
	v_rsq_f32_e32 v146, v146
	s_nop 0
	v_mul_f32_e32 v147, 0x45800000, v146
	v_cndmask_b32_e32 v148, v146, v147, vcc
	v_ffbh_u32_e32 v146, v145
	v_min_u32_e32 v146, 32, v146
	v_lshlrev_b64 v[144:145], v146, v[144:145]
	v_min_u32_e32 v144, 1, v144
	v_or_b32_e32 v144, v145, v144
	v_cvt_f32_u32_e32 v144, v144
	v_sub_u32_e32 v145, 32, v146
	v_ldexp_f32 v145, v144, v145
	v_ffbh_u32_e32 v144, v143
	v_min_u32_e32 v144, 32, v144
	v_lshlrev_b64 v[142:143], v144, v[142:143]
	v_min_u32_e32 v142, 1, v142
	v_or_b32_e32 v142, v143, v142
	v_cvt_f32_u32_e32 v142, v142
	v_sub_u32_e32 v143, 32, v144
	v_ldexp_f32 v144, v142, v143
	v_pk_fma_f32 v[142:143], v[144:145], s[48:49], v[164:165] op_sel_hi:[1,0,0]
	s_nop 0
	v_mul_f32_e32 v144, 0x4b800000, v143
	v_cmp_gt_f32_e64 s[36:37], s96, v143
	v_cmp_gt_f32_e32 vcc, s96, v142
	s_nop 0
	v_cndmask_b32_e64 v143, v143, v144, s[36:37]
	v_rsq_f32_e32 v143, v143
	s_nop 0
	v_mul_f32_e32 v144, 0x45800000, v143
	v_cndmask_b32_e64 v147, v143, v144, s[36:37]
	s_ashr_i32 s36, s83, 2
	s_ashr_i32 s37, s36, 31
	s_lshl_b64 s[36:37], s[36:37], 25
	s_add_u32 s29, s60, s36
	s_addc_u32 s36, s61, s37
	s_lshl_b32 s37, s83, 9
	s_and_b32 s37, s37, 0x600
	s_add_u32 s29, s29, s37
	s_addc_u32 s37, s36, 0
	s_add_u32 s36, s29, s82
	s_addc_u32 s37, s37, 0
	v_lshl_add_u64 v[144:145], s[36:37], 0, v[0:1]
	v_mul_f32_e32 v0, 0xbfb8aa3b, v155
	v_pk_mul_f32 v[122:123], v[0:1], v[122:123] op_sel_hi:[0,1]
	v_exp_f32_e32 v122, v122
	v_pk_mul_f32 v[124:125], v[0:1], v[124:125] op_sel_hi:[0,1]
	v_pk_mul_f32 v[128:129], v[0:1], v[128:129] op_sel_hi:[0,1]
	v_pk_mul_f32 v[126:127], v[0:1], v[126:127] op_sel_hi:[0,1]
	v_add_f32_e32 v122, 1.0, v122
	v_rcp_f32_e32 v152, v122
	v_exp_f32_e32 v122, v123
	v_exp_f32_e32 v126, v126
	v_exp_f32_e32 v127, v127
	v_exp_f32_e32 v128, v128
	v_add_f32_e32 v122, 1.0, v122
	v_rcp_f32_e32 v153, v122
	v_exp_f32_e32 v122, v124
	v_exp_f32_e32 v129, v129
	v_mul_f32_e32 v143, 0x4b800000, v142
	v_cndmask_b32_e32 v142, v142, v143, vcc
	v_add_f32_e32 v122, 1.0, v122
	v_rcp_f32_e32 v155, v122
	v_exp_f32_e32 v122, v125
	v_rsq_f32_e32 v142, v142
	v_add_f32_e32 v126, 1.0, v126
	v_add_f32_e32 v127, 1.0, v127
	v_add_f32_e32 v128, 1.0, v128
	v_add_f32_e32 v129, 1.0, v129
	v_add_f32_e32 v122, 1.0, v122
	v_pk_mul_f32 v[114:115], v[0:1], v[114:115] op_sel_hi:[0,1]
	v_rcp_f32_e32 v126, v126
	v_rcp_f32_e32 v127, v127
	v_rcp_f32_e32 v128, v128
	v_rcp_f32_e32 v129, v129
	v_rcp_f32_e32 v125, v122
	v_pk_mul_f32 v[120:121], v[0:1], v[120:121] op_sel_hi:[0,1]
	v_pk_mul_f32 v[118:119], v[0:1], v[118:119] op_sel_hi:[0,1]
	v_pk_mul_f32 v[116:117], v[0:1], v[116:117] op_sel_hi:[0,1]
	v_exp_f32_e32 v0, v114
	v_exp_f32_e32 v114, v115
	v_mul_f32_e32 v143, 0x45800000, v142
	v_cndmask_b32_e32 v146, v142, v143, vcc
	v_lshlrev_b64 v[142:143], 11, v[158:159]
	v_lshl_add_u64 v[142:143], v[144:145], 0, v[142:143]
	v_cvt_pk_bf16_f32 v122, v126, v127
	v_cvt_pk_bf16_f32 v123, v128, v129
	v_cvt_pk_bf16_f32 v124, v152, v153
	v_cvt_pk_bf16_f32 v125, v155, v125
	v_add_f32_e32 v114, 1.0, v114
	global_store_dwordx4 v[142:143], v[122:125], off sc1
	v_add_f32_e32 v0, 1.0, v0
	v_rcp_f32_e32 v0, v0
	v_rcp_f32_e32 v122, v114
	v_exp_f32_e32 v114, v116
	v_exp_f32_e32 v118, v118
	v_exp_f32_e32 v119, v119
	v_exp_f32_e32 v120, v120
	v_add_f32_e32 v114, 1.0, v114
	v_exp_f32_e32 v121, v121
	v_rcp_f32_e32 v123, v114
	v_exp_f32_e32 v114, v117
	v_cvt_pk_bf16_f32 v116, v0, v122
	v_mul_f32_e32 v0, 0xbfb8aa3b, v154
	v_add_f32_e32 v118, 1.0, v118
	v_add_f32_e32 v119, 1.0, v119
	v_add_f32_e32 v120, 1.0, v120
	v_add_f32_e32 v121, 1.0, v121
	v_add_f32_e32 v114, 1.0, v114
	v_pk_mul_f32 v[106:107], v[0:1], v[106:107] op_sel_hi:[0,1]
	v_rcp_f32_e32 v118, v118
	v_rcp_f32_e32 v119, v119
	v_rcp_f32_e32 v120, v120
	v_rcp_f32_e32 v121, v121
	v_rcp_f32_e32 v117, v114
	v_exp_f32_e32 v106, v106
	v_cvt_pk_bf16_f32 v114, v118, v119
	v_cvt_pk_bf16_f32 v115, v120, v121
	v_cvt_pk_bf16_f32 v117, v123, v117
	v_add_f32_e32 v106, 1.0, v106
	global_store_dwordx4 v[142:143], v[114:117], off offset:256 sc1
	v_pk_mul_f32 v[108:109], v[0:1], v[108:109] op_sel_hi:[0,1]
	v_pk_mul_f32 v[112:113], v[0:1], v[112:113] op_sel_hi:[0,1]
	v_rcp_f32_e32 v116, v106
	v_exp_f32_e32 v106, v107
	v_pk_mul_f32 v[110:111], v[0:1], v[110:111] op_sel_hi:[0,1]
	v_exp_f32_e32 v110, v110
	v_exp_f32_e32 v111, v111
	v_add_f32_e32 v106, 1.0, v106
	v_rcp_f32_e32 v117, v106
	v_exp_f32_e32 v106, v108
	v_exp_f32_e32 v112, v112
	v_exp_f32_e32 v113, v113
	v_add_f32_e32 v110, 1.0, v110
	v_add_f32_e32 v106, 1.0, v106
	v_rcp_f32_e32 v118, v106
	v_exp_f32_e32 v106, v109
	v_add_f32_e32 v111, 1.0, v111
	v_add_f32_e32 v112, 1.0, v112
	v_add_f32_e32 v113, 1.0, v113
	v_add_f32_e32 v106, 1.0, v106
	v_pk_mul_f32 v[98:99], v[0:1], v[98:99] op_sel_hi:[0,1]
	v_rcp_f32_e32 v110, v110
	v_rcp_f32_e32 v111, v111
	v_rcp_f32_e32 v112, v112
	v_rcp_f32_e32 v113, v113
	v_rcp_f32_e32 v109, v106
	v_pk_mul_f32 v[104:105], v[0:1], v[104:105] op_sel_hi:[0,1]
	v_pk_mul_f32 v[102:103], v[0:1], v[102:103] op_sel_hi:[0,1]
	v_pk_mul_f32 v[100:101], v[0:1], v[100:101] op_sel_hi:[0,1]
	v_exp_f32_e32 v0, v98
	v_exp_f32_e32 v98, v99
	v_or_b32_e32 v114, 16, v158
	v_ashrrev_i32_e32 v115, 31, v114
	v_lshlrev_b64 v[114:115], 11, v[114:115]
	v_lshl_add_u64 v[114:115], v[144:145], 0, v[114:115]
	v_cvt_pk_bf16_f32 v106, v110, v111
	v_cvt_pk_bf16_f32 v107, v112, v113
	v_cvt_pk_bf16_f32 v108, v116, v117
	v_cvt_pk_bf16_f32 v109, v118, v109
	v_add_f32_e32 v98, 1.0, v98
	global_store_dwordx4 v[114:115], v[106:109], off sc1
	v_add_f32_e32 v0, 1.0, v0
	v_rcp_f32_e32 v0, v0
	v_rcp_f32_e32 v106, v98
	v_exp_f32_e32 v98, v100
	v_exp_f32_e32 v102, v102
	v_exp_f32_e32 v103, v103
	v_exp_f32_e32 v104, v104
	v_add_f32_e32 v98, 1.0, v98
	v_exp_f32_e32 v105, v105
	v_rcp_f32_e32 v107, v98
	v_exp_f32_e32 v98, v101
	v_cvt_pk_bf16_f32 v100, v0, v106
	v_mul_f32_e32 v0, 0xbfb8aa3b, v151
	v_add_f32_e32 v102, 1.0, v102
	v_add_f32_e32 v103, 1.0, v103
	v_add_f32_e32 v104, 1.0, v104
	v_add_f32_e32 v105, 1.0, v105
	v_add_f32_e32 v98, 1.0, v98
	v_pk_mul_f32 v[90:91], v[0:1], v[90:91] op_sel_hi:[0,1]
	v_rcp_f32_e32 v102, v102
	v_rcp_f32_e32 v103, v103
	v_rcp_f32_e32 v104, v104
	v_rcp_f32_e32 v105, v105
	v_rcp_f32_e32 v101, v98
	v_exp_f32_e32 v90, v90
	v_cvt_pk_bf16_f32 v98, v102, v103
	v_cvt_pk_bf16_f32 v99, v104, v105
	v_cvt_pk_bf16_f32 v101, v107, v101
	v_add_f32_e32 v90, 1.0, v90
	global_store_dwordx4 v[114:115], v[98:101], off offset:256 sc1
	v_pk_mul_f32 v[92:93], v[0:1], v[92:93] op_sel_hi:[0,1]
	v_pk_mul_f32 v[96:97], v[0:1], v[96:97] op_sel_hi:[0,1]
	v_rcp_f32_e32 v100, v90
	v_exp_f32_e32 v90, v91
	v_pk_mul_f32 v[94:95], v[0:1], v[94:95] op_sel_hi:[0,1]
	v_exp_f32_e32 v94, v94
	v_exp_f32_e32 v95, v95
	v_add_f32_e32 v90, 1.0, v90
	v_rcp_f32_e32 v101, v90
	v_exp_f32_e32 v90, v92
	v_exp_f32_e32 v96, v96
	v_exp_f32_e32 v97, v97
	v_add_f32_e32 v94, 1.0, v94
	v_add_f32_e32 v90, 1.0, v90
	v_rcp_f32_e32 v102, v90
	v_exp_f32_e32 v90, v93
	v_add_f32_e32 v95, 1.0, v95
	v_add_f32_e32 v96, 1.0, v96
	v_add_f32_e32 v97, 1.0, v97
	v_add_f32_e32 v90, 1.0, v90
	v_pk_mul_f32 v[82:83], v[0:1], v[82:83] op_sel_hi:[0,1]
	v_rcp_f32_e32 v94, v94
	v_rcp_f32_e32 v95, v95
	v_rcp_f32_e32 v96, v96
	v_rcp_f32_e32 v97, v97
	v_rcp_f32_e32 v93, v90
	v_pk_mul_f32 v[88:89], v[0:1], v[88:89] op_sel_hi:[0,1]
	v_pk_mul_f32 v[86:87], v[0:1], v[86:87] op_sel_hi:[0,1]
	v_pk_mul_f32 v[84:85], v[0:1], v[84:85] op_sel_hi:[0,1]
	v_exp_f32_e32 v0, v82
	v_exp_f32_e32 v82, v83
	v_or_b32_e32 v98, 32, v158
	v_ashrrev_i32_e32 v99, 31, v98
	v_lshlrev_b64 v[98:99], 11, v[98:99]
	v_lshl_add_u64 v[98:99], v[144:145], 0, v[98:99]
	v_cvt_pk_bf16_f32 v90, v94, v95
	v_cvt_pk_bf16_f32 v91, v96, v97
	v_cvt_pk_bf16_f32 v92, v100, v101
	v_cvt_pk_bf16_f32 v93, v102, v93
	v_add_f32_e32 v82, 1.0, v82
	global_store_dwordx4 v[98:99], v[90:93], off sc1
	v_add_f32_e32 v0, 1.0, v0
	v_rcp_f32_e32 v0, v0
	v_rcp_f32_e32 v90, v82
	v_exp_f32_e32 v82, v84
	v_exp_f32_e32 v86, v86
	v_exp_f32_e32 v87, v87
	v_exp_f32_e32 v88, v88
	v_add_f32_e32 v82, 1.0, v82
	v_exp_f32_e32 v89, v89
	v_rcp_f32_e32 v91, v82
	v_exp_f32_e32 v82, v85
	v_cvt_pk_bf16_f32 v84, v0, v90
	v_mul_f32_e32 v0, 0xbfb8aa3b, v150
	v_add_f32_e32 v86, 1.0, v86
	v_add_f32_e32 v87, 1.0, v87
	v_add_f32_e32 v88, 1.0, v88
	v_add_f32_e32 v89, 1.0, v89
	v_add_f32_e32 v82, 1.0, v82
	v_pk_mul_f32 v[74:75], v[0:1], v[74:75] op_sel_hi:[0,1]
	v_rcp_f32_e32 v86, v86
	v_rcp_f32_e32 v87, v87
	v_rcp_f32_e32 v88, v88
	v_rcp_f32_e32 v89, v89
	v_rcp_f32_e32 v85, v82
	v_exp_f32_e32 v74, v74
	v_cvt_pk_bf16_f32 v82, v86, v87
	v_cvt_pk_bf16_f32 v83, v88, v89
	v_cvt_pk_bf16_f32 v85, v91, v85
	v_add_f32_e32 v74, 1.0, v74
	global_store_dwordx4 v[98:99], v[82:85], off offset:256 sc1
	v_pk_mul_f32 v[76:77], v[0:1], v[76:77] op_sel_hi:[0,1]
	v_pk_mul_f32 v[80:81], v[0:1], v[80:81] op_sel_hi:[0,1]
	v_rcp_f32_e32 v84, v74
	v_exp_f32_e32 v74, v75
	v_pk_mul_f32 v[78:79], v[0:1], v[78:79] op_sel_hi:[0,1]
	v_exp_f32_e32 v78, v78
	v_exp_f32_e32 v79, v79
	v_add_f32_e32 v74, 1.0, v74
	v_rcp_f32_e32 v85, v74
	v_exp_f32_e32 v74, v76
	v_exp_f32_e32 v80, v80
	v_exp_f32_e32 v81, v81
	v_add_f32_e32 v78, 1.0, v78
	v_add_f32_e32 v74, 1.0, v74
	v_rcp_f32_e32 v86, v74
	v_exp_f32_e32 v74, v77
	v_add_f32_e32 v79, 1.0, v79
	v_add_f32_e32 v80, 1.0, v80
	v_add_f32_e32 v81, 1.0, v81
	v_add_f32_e32 v74, 1.0, v74
	v_pk_mul_f32 v[66:67], v[0:1], v[66:67] op_sel_hi:[0,1]
	v_rcp_f32_e32 v78, v78
	v_rcp_f32_e32 v79, v79
	v_rcp_f32_e32 v80, v80
	v_rcp_f32_e32 v81, v81
	v_rcp_f32_e32 v77, v74
	v_pk_mul_f32 v[72:73], v[0:1], v[72:73] op_sel_hi:[0,1]
	v_pk_mul_f32 v[70:71], v[0:1], v[70:71] op_sel_hi:[0,1]
	v_pk_mul_f32 v[68:69], v[0:1], v[68:69] op_sel_hi:[0,1]
	v_exp_f32_e32 v0, v66
	v_exp_f32_e32 v66, v67
	v_or_b32_e32 v82, 48, v158
	v_ashrrev_i32_e32 v83, 31, v82
	v_lshlrev_b64 v[82:83], 11, v[82:83]
	v_lshl_add_u64 v[82:83], v[144:145], 0, v[82:83]
	v_cvt_pk_bf16_f32 v74, v78, v79
	v_cvt_pk_bf16_f32 v75, v80, v81
	v_cvt_pk_bf16_f32 v76, v84, v85
	v_cvt_pk_bf16_f32 v77, v86, v77
	v_add_f32_e32 v66, 1.0, v66
	global_store_dwordx4 v[82:83], v[74:77], off sc1
	v_add_f32_e32 v0, 1.0, v0
	v_rcp_f32_e32 v0, v0
	v_rcp_f32_e32 v74, v66
	v_exp_f32_e32 v66, v68
	v_exp_f32_e32 v70, v70
	v_exp_f32_e32 v71, v71
	v_exp_f32_e32 v72, v72
	v_add_f32_e32 v66, 1.0, v66
	v_exp_f32_e32 v73, v73
	v_rcp_f32_e32 v75, v66
	v_exp_f32_e32 v66, v69
	v_cvt_pk_bf16_f32 v68, v0, v74
	v_mul_f32_e32 v0, 0xbfb8aa3b, v149
	v_add_f32_e32 v70, 1.0, v70
	v_add_f32_e32 v71, 1.0, v71
	v_add_f32_e32 v72, 1.0, v72
	v_add_f32_e32 v73, 1.0, v73
	v_add_f32_e32 v66, 1.0, v66
	v_pk_mul_f32 v[58:59], v[0:1], v[58:59] op_sel_hi:[0,1]
	v_rcp_f32_e32 v70, v70
	v_rcp_f32_e32 v71, v71
	v_rcp_f32_e32 v72, v72
	v_rcp_f32_e32 v73, v73
	v_rcp_f32_e32 v69, v66
	v_exp_f32_e32 v58, v58
	v_cvt_pk_bf16_f32 v66, v70, v71
	v_cvt_pk_bf16_f32 v67, v72, v73
	v_cvt_pk_bf16_f32 v69, v75, v69
	v_add_f32_e32 v58, 1.0, v58
	global_store_dwordx4 v[82:83], v[66:69], off offset:256 sc1
	v_pk_mul_f32 v[60:61], v[0:1], v[60:61] op_sel_hi:[0,1]
	v_pk_mul_f32 v[62:63], v[0:1], v[62:63] op_sel_hi:[0,1]
	v_rcp_f32_e32 v68, v58
	v_exp_f32_e32 v58, v59
	v_pk_mul_f32 v[64:65], v[0:1], v[64:65] op_sel_hi:[0,1]
	v_exp_f32_e32 v62, v62
	v_exp_f32_e32 v63, v63
	v_add_f32_e32 v58, 1.0, v58
	v_rcp_f32_e32 v69, v58
	v_exp_f32_e32 v58, v60
	v_exp_f32_e32 v64, v64
	v_exp_f32_e32 v65, v65
	v_add_f32_e32 v62, 1.0, v62
	v_add_f32_e32 v58, 1.0, v58
	v_rcp_f32_e32 v70, v58
	v_exp_f32_e32 v58, v61
	v_add_f32_e32 v63, 1.0, v63
	v_rcp_f32_e32 v62, v62
	v_rcp_f32_e32 v63, v63
	v_add_f32_e32 v64, 1.0, v64
	v_add_f32_e32 v65, 1.0, v65
	v_add_f32_e32 v58, 1.0, v58
	v_pk_mul_f32 v[50:51], v[0:1], v[50:51] op_sel_hi:[0,1]
	v_rcp_f32_e32 v64, v64
	v_rcp_f32_e32 v65, v65
	v_rcp_f32_e32 v61, v58
	v_pk_mul_f32 v[56:57], v[0:1], v[56:57] op_sel_hi:[0,1]
	v_pk_mul_f32 v[54:55], v[0:1], v[54:55] op_sel_hi:[0,1]
	v_pk_mul_f32 v[52:53], v[0:1], v[52:53] op_sel_hi:[0,1]
	v_exp_f32_e32 v0, v50
	v_exp_f32_e32 v50, v51
	s_mov_b32 s29, 0x40000
	v_cvt_pk_bf16_f32 v58, v62, v63
	v_add_co_u32_e32 v62, vcc, s29, v142
	v_cvt_pk_bf16_f32 v59, v64, v65
	v_cvt_pk_bf16_f32 v60, v68, v69
	v_cvt_pk_bf16_f32 v61, v70, v61
	v_addc_co_u32_e32 v63, vcc, 0, v143, vcc
	v_add_f32_e32 v50, 1.0, v50
	global_store_dwordx4 v[62:63], v[58:61], off sc1
	v_add_f32_e32 v0, 1.0, v0
	v_rcp_f32_e32 v0, v0
	v_rcp_f32_e32 v58, v50
	v_exp_f32_e32 v50, v52
	v_exp_f32_e32 v54, v54
	v_exp_f32_e32 v55, v55
	v_exp_f32_e32 v56, v56
	v_add_f32_e32 v50, 1.0, v50
	v_exp_f32_e32 v57, v57
	v_rcp_f32_e32 v59, v50
	v_exp_f32_e32 v50, v53
	v_cvt_pk_bf16_f32 v52, v0, v58
	v_mul_f32_e32 v0, 0xbfb8aa3b, v148
	v_add_f32_e32 v54, 1.0, v54
	v_add_f32_e32 v55, 1.0, v55
	v_add_f32_e32 v56, 1.0, v56
	v_add_f32_e32 v57, 1.0, v57
	v_add_f32_e32 v50, 1.0, v50
	v_pk_mul_f32 v[42:43], v[0:1], v[42:43] op_sel_hi:[0,1]
	v_rcp_f32_e32 v54, v54
	v_rcp_f32_e32 v55, v55
	v_rcp_f32_e32 v56, v56
	v_rcp_f32_e32 v57, v57
	v_rcp_f32_e32 v53, v50
	v_exp_f32_e32 v42, v42
	v_lshl_add_u64 v[66:67], v[142:143], 0, s[20:21]
	v_cvt_pk_bf16_f32 v50, v54, v55
	v_cvt_pk_bf16_f32 v51, v56, v57
	v_cvt_pk_bf16_f32 v53, v59, v53
	v_add_f32_e32 v42, 1.0, v42
	global_store_dwordx4 v[66:67], v[50:53], off offset:256 sc1
	v_pk_mul_f32 v[44:45], v[0:1], v[44:45] op_sel_hi:[0,1]
	v_pk_mul_f32 v[46:47], v[0:1], v[46:47] op_sel_hi:[0,1]
	v_rcp_f32_e32 v52, v42
	v_exp_f32_e32 v42, v43
	v_pk_mul_f32 v[48:49], v[0:1], v[48:49] op_sel_hi:[0,1]
	v_exp_f32_e32 v46, v46
	v_exp_f32_e32 v47, v47
	v_add_f32_e32 v42, 1.0, v42
	v_rcp_f32_e32 v53, v42
	v_exp_f32_e32 v42, v44
	v_exp_f32_e32 v48, v48
	v_exp_f32_e32 v49, v49
	v_add_f32_e32 v46, 1.0, v46
	v_add_f32_e32 v42, 1.0, v42
	v_rcp_f32_e32 v54, v42
	v_exp_f32_e32 v42, v45
	v_add_f32_e32 v47, 1.0, v47
	v_rcp_f32_e32 v46, v46
	v_rcp_f32_e32 v47, v47
	v_add_f32_e32 v48, 1.0, v48
	v_add_f32_e32 v49, 1.0, v49
	v_add_f32_e32 v42, 1.0, v42
	v_pk_mul_f32 v[34:35], v[0:1], v[34:35] op_sel_hi:[0,1]
	v_rcp_f32_e32 v48, v48
	v_rcp_f32_e32 v49, v49
	v_rcp_f32_e32 v45, v42
	v_pk_mul_f32 v[40:41], v[0:1], v[40:41] op_sel_hi:[0,1]
	v_pk_mul_f32 v[38:39], v[0:1], v[38:39] op_sel_hi:[0,1]
	v_pk_mul_f32 v[36:37], v[0:1], v[36:37] op_sel_hi:[0,1]
	v_exp_f32_e32 v0, v34
	v_exp_f32_e32 v34, v35
	s_mov_b32 s29, 0x48000
	v_cvt_pk_bf16_f32 v42, v46, v47
	v_add_co_u32_e32 v46, vcc, s29, v142
	v_cvt_pk_bf16_f32 v43, v48, v49
	v_cvt_pk_bf16_f32 v44, v52, v53
	v_cvt_pk_bf16_f32 v45, v54, v45
	v_addc_co_u32_e32 v47, vcc, 0, v143, vcc
	v_add_f32_e32 v34, 1.0, v34
	global_store_dwordx4 v[46:47], v[42:45], off sc1
	v_add_f32_e32 v0, 1.0, v0
	v_rcp_f32_e32 v0, v0
	v_rcp_f32_e32 v42, v34
	v_exp_f32_e32 v34, v36
	v_exp_f32_e32 v38, v38
	v_exp_f32_e32 v39, v39
	v_exp_f32_e32 v40, v40
	v_add_f32_e32 v34, 1.0, v34
	v_exp_f32_e32 v41, v41
	v_rcp_f32_e32 v43, v34
	v_exp_f32_e32 v34, v37
	v_cvt_pk_bf16_f32 v36, v0, v42
	v_mul_f32_e32 v0, 0xbfb8aa3b, v147
	v_add_f32_e32 v38, 1.0, v38
	v_add_f32_e32 v39, 1.0, v39
	v_add_f32_e32 v40, 1.0, v40
	v_add_f32_e32 v41, 1.0, v41
	v_add_f32_e32 v34, 1.0, v34
	v_pk_mul_f32 v[26:27], v[0:1], v[26:27] op_sel_hi:[0,1]
	v_rcp_f32_e32 v38, v38
	v_rcp_f32_e32 v39, v39
	v_rcp_f32_e32 v40, v40
	v_rcp_f32_e32 v41, v41
	v_rcp_f32_e32 v37, v34
	v_exp_f32_e32 v26, v26
	s_mov_b64 s[36:37], 0x48000
	v_lshl_add_u64 v[50:51], v[142:143], 0, s[36:37]
	v_cvt_pk_bf16_f32 v34, v38, v39
	v_cvt_pk_bf16_f32 v35, v40, v41
	v_cvt_pk_bf16_f32 v37, v43, v37
	v_add_f32_e32 v26, 1.0, v26
	global_store_dwordx4 v[50:51], v[34:37], off offset:256 sc1
	v_pk_mul_f32 v[28:29], v[0:1], v[28:29] op_sel_hi:[0,1]
	v_pk_mul_f32 v[30:31], v[0:1], v[30:31] op_sel_hi:[0,1]
	v_rcp_f32_e32 v36, v26
	v_exp_f32_e32 v26, v27
	v_pk_mul_f32 v[32:33], v[0:1], v[32:33] op_sel_hi:[0,1]
	v_exp_f32_e32 v30, v30
	v_exp_f32_e32 v31, v31
	v_add_f32_e32 v26, 1.0, v26
	v_rcp_f32_e32 v37, v26
	v_exp_f32_e32 v26, v28
	v_exp_f32_e32 v32, v32
	v_exp_f32_e32 v33, v33
	v_add_f32_e32 v30, 1.0, v30
	v_add_f32_e32 v26, 1.0, v26
	v_rcp_f32_e32 v38, v26
	v_exp_f32_e32 v26, v29
	v_add_f32_e32 v31, 1.0, v31
	v_rcp_f32_e32 v30, v30
	v_rcp_f32_e32 v31, v31
	v_add_f32_e32 v32, 1.0, v32
	v_add_f32_e32 v33, 1.0, v33
	v_add_f32_e32 v26, 1.0, v26
	v_pk_mul_f32 v[18:19], v[0:1], v[18:19] op_sel_hi:[0,1]
	v_rcp_f32_e32 v32, v32
	v_rcp_f32_e32 v33, v33
	v_rcp_f32_e32 v29, v26
	v_pk_mul_f32 v[24:25], v[0:1], v[24:25] op_sel_hi:[0,1]
	v_pk_mul_f32 v[22:23], v[0:1], v[22:23] op_sel_hi:[0,1]
	v_pk_mul_f32 v[20:21], v[0:1], v[20:21] op_sel_hi:[0,1]
	v_exp_f32_e32 v0, v18
	v_exp_f32_e32 v18, v19
	s_mov_b32 s29, 0x50000
	v_cvt_pk_bf16_f32 v26, v30, v31
	v_add_co_u32_e32 v30, vcc, s29, v142
	v_cvt_pk_bf16_f32 v27, v32, v33
	v_cvt_pk_bf16_f32 v28, v36, v37
	v_cvt_pk_bf16_f32 v29, v38, v29
	v_addc_co_u32_e32 v31, vcc, 0, v143, vcc
	v_add_f32_e32 v18, 1.0, v18
	global_store_dwordx4 v[30:31], v[26:29], off sc1
	v_add_f32_e32 v0, 1.0, v0
	v_rcp_f32_e32 v0, v0
	v_rcp_f32_e32 v26, v18
	v_exp_f32_e32 v18, v20
	v_exp_f32_e32 v22, v22
	v_exp_f32_e32 v23, v23
	v_exp_f32_e32 v24, v24
	v_add_f32_e32 v18, 1.0, v18
	v_exp_f32_e32 v25, v25
	v_rcp_f32_e32 v27, v18
	v_exp_f32_e32 v18, v21
	v_cvt_pk_bf16_f32 v20, v0, v26
	v_mul_f32_e32 v0, 0xbfb8aa3b, v146
	v_add_f32_e32 v22, 1.0, v22
	v_add_f32_e32 v23, 1.0, v23
	v_add_f32_e32 v24, 1.0, v24
	v_add_f32_e32 v25, 1.0, v25
	v_add_f32_e32 v18, 1.0, v18
	v_pk_mul_f32 v[10:11], v[0:1], v[10:11] op_sel_hi:[0,1]
	v_rcp_f32_e32 v22, v22
	v_rcp_f32_e32 v23, v23
	v_rcp_f32_e32 v24, v24
	v_rcp_f32_e32 v25, v25
	v_rcp_f32_e32 v21, v18
	v_exp_f32_e32 v10, v10
	v_lshl_add_u64 v[34:35], v[142:143], 0, s[22:23]
	v_cvt_pk_bf16_f32 v18, v22, v23
	v_cvt_pk_bf16_f32 v19, v24, v25
	v_cvt_pk_bf16_f32 v21, v27, v21
	v_add_f32_e32 v10, 1.0, v10
	global_store_dwordx4 v[34:35], v[18:21], off offset:256 sc1
	v_pk_mul_f32 v[12:13], v[0:1], v[12:13] op_sel_hi:[0,1]
	v_pk_mul_f32 v[14:15], v[0:1], v[14:15] op_sel_hi:[0,1]
	v_rcp_f32_e32 v20, v10
	v_exp_f32_e32 v10, v11
	v_pk_mul_f32 v[16:17], v[0:1], v[16:17] op_sel_hi:[0,1]
	v_exp_f32_e32 v14, v14
	v_exp_f32_e32 v15, v15
	v_add_f32_e32 v10, 1.0, v10
	v_rcp_f32_e32 v21, v10
	v_exp_f32_e32 v10, v12
	v_exp_f32_e32 v16, v16
	v_exp_f32_e32 v17, v17
	v_add_f32_e32 v14, 1.0, v14
	v_add_f32_e32 v10, 1.0, v10
	v_rcp_f32_e32 v22, v10
	v_exp_f32_e32 v10, v13
	v_add_f32_e32 v15, 1.0, v15
	v_rcp_f32_e32 v14, v14
	v_rcp_f32_e32 v15, v15
	v_add_f32_e32 v16, 1.0, v16
	v_add_f32_e32 v17, 1.0, v17
	v_add_f32_e32 v10, 1.0, v10
	v_pk_mul_f32 v[2:3], v[0:1], v[2:3] op_sel_hi:[0,1]
	v_rcp_f32_e32 v16, v16
	v_rcp_f32_e32 v17, v17
	v_rcp_f32_e32 v13, v10
	v_pk_mul_f32 v[8:9], v[0:1], v[8:9] op_sel_hi:[0,1]
	v_pk_mul_f32 v[6:7], v[0:1], v[6:7] op_sel_hi:[0,1]
	v_pk_mul_f32 v[4:5], v[0:1], v[4:5] op_sel_hi:[0,1]
	v_exp_f32_e32 v0, v2
	v_exp_f32_e32 v2, v3
	s_mov_b32 s29, 0x58000
	v_cvt_pk_bf16_f32 v10, v14, v15
	v_add_co_u32_e32 v14, vcc, s29, v142
	v_cvt_pk_bf16_f32 v11, v16, v17
	v_cvt_pk_bf16_f32 v12, v20, v21
	v_cvt_pk_bf16_f32 v13, v22, v13
	v_addc_co_u32_e32 v15, vcc, 0, v143, vcc
	v_add_f32_e32 v2, 1.0, v2
	global_store_dwordx4 v[14:15], v[10:13], off sc1
	v_exp_f32_e32 v6, v6
	v_exp_f32_e32 v7, v7
	v_rcp_f32_e32 v10, v2
	v_exp_f32_e32 v2, v4
	v_exp_f32_e32 v8, v8
	v_exp_f32_e32 v9, v9
	v_add_f32_e32 v6, 1.0, v6
	v_add_f32_e32 v2, 1.0, v2
	v_rcp_f32_e32 v11, v2
	v_exp_f32_e32 v2, v5
	v_add_f32_e32 v7, 1.0, v7
	v_add_f32_e32 v8, 1.0, v8
	v_add_f32_e32 v9, 1.0, v9
	v_add_f32_e32 v0, 1.0, v0
	v_add_f32_e32 v2, 1.0, v2
	v_rcp_f32_e32 v6, v6
	v_rcp_f32_e32 v7, v7
	v_rcp_f32_e32 v8, v8
	v_rcp_f32_e32 v9, v9
	v_rcp_f32_e32 v0, v0
	v_rcp_f32_e32 v5, v2
	s_mov_b64 s[36:37], 0x58000
	v_lshl_add_u64 v[18:19], v[142:143], 0, s[36:37]
	v_cvt_pk_bf16_f32 v2, v6, v7
	v_cvt_pk_bf16_f32 v3, v8, v9
	v_cvt_pk_bf16_f32 v4, v0, v10
	v_cvt_pk_bf16_f32 v5, v11, v5
	s_mov_b64 s[36:37], -1
	s_andn2_b64 vcc, exec, s[46:47]
	global_store_dwordx4 v[18:19], v[2:5], off offset:256 sc1
	s_cbranch_vccnz .LBB0_1054
	s_nop 0
	v_lshl_add_u32 v2, s38, 8, v160
	v_ashrrev_i32_e32 v3, 31, v2
	v_lshl_add_u64 v[2:3], v[2:3], 3, s[0:1]
	global_load_dwordx2 v[156:157], v[2:3], off nt
	global_load_dwordx2 v[154:155], v[2:3], off offset:128 nt
	global_load_dwordx2 v[152:153], v[2:3], off offset:256 nt
	global_load_dwordx2 v[150:151], v[2:3], off offset:384 nt
	global_load_dwordx2 v[148:149], v[2:3], off offset:1024 nt
	global_load_dwordx2 v[146:147], v[2:3], off offset:1152 nt
	global_load_dwordx2 v[144:145], v[2:3], off offset:1280 nt
	global_load_dwordx2 v[142:143], v[2:3], off offset:1408 nt
	s_andn2_b64 vcc, exec, s[14:15]
	s_cbranch_vccnz .LBB0_1053
	s_barrier
	s_branch .LBB0_1053

.LBB0_2009:
	s_waitcnt vmcnt(8)
	v_ffbh_u32_e32 v161, v157
	v_min_u32_e32 v161, 32, v161
	v_lshlrev_b64 v[156:157], v161, v[156:157]
	v_min_u32_e32 v156, 1, v156
	v_or_b32_e32 v156, v157, v156
	v_cvt_f32_u32_e32 v156, v156
	v_sub_u32_e32 v157, 32, v161
	s_mov_b32 s36, 0x358637bd
	v_mov_b64_e32 v[166:167], s[36:37]
	v_ldexp_f32 v157, v156, v157
	v_ffbh_u32_e32 v156, v155
	v_min_u32_e32 v156, 32, v156
	v_lshlrev_b64 v[154:155], v156, v[154:155]
	v_min_u32_e32 v154, 1, v154
	v_or_b32_e32 v154, v155, v154
	v_cvt_f32_u32_e32 v154, v154
	v_sub_u32_e32 v155, 32, v156
	s_mov_b32 s40, 0x32800000
	s_mov_b32 s29, -1
	v_ldexp_f32 v156, v154, v155
	v_pk_fma_f32 v[154:155], v[156:157], s[40:41], v[166:167] op_sel_hi:[1,0,0]
	s_movk_i32 s95, 0x100
	v_mul_f32_e32 v156, 0x4b800000, v155
	v_cmp_gt_f32_e64 s[36:37], s96, v155
	v_cmp_gt_f32_e32 vcc, s96, v154
	v_mbcnt_lo_u32_b32 v0, s29, 0
	v_cndmask_b32_e64 v155, v155, v156, s[36:37]
	v_rsq_f32_e32 v155, v155
	v_mbcnt_hi_u32_b32 v159, s29, v0
	s_lshl_b32 s29, s58, 8
	v_lshrrev_b32_e32 v160, 1, v159
	v_mul_f32_e32 v156, 0x45800000, v155
	v_cndmask_b32_e64 v156, v155, v156, s[36:37]
	v_mul_f32_e32 v155, 0x4b800000, v154
	v_cndmask_b32_e32 v154, v154, v155, vcc
	v_rsq_f32_e32 v154, v154
	v_and_b32_e32 v0, 15, v159
	s_add_i32 s29, s29, s34
	v_and_b32_e32 v160, 56, v160
	v_mul_f32_e32 v155, 0x45800000, v154
	v_cndmask_b32_e32 v154, v154, v155, vcc
	v_ffbh_u32_e32 v155, v153
	v_min_u32_e32 v155, 32, v155
	v_lshlrev_b64 v[152:153], v155, v[152:153]
	v_min_u32_e32 v152, 1, v152
	v_or_b32_e32 v152, v153, v152
	v_cvt_f32_u32_e32 v152, v152
	v_sub_u32_e32 v153, 32, v155
	v_or_b32_e32 v158, s29, v0
	v_add_u32_e32 v160, s85, v160
	v_ldexp_f32 v153, v152, v153
	v_ffbh_u32_e32 v152, v151
	v_min_u32_e32 v152, 32, v152
	v_lshlrev_b64 v[150:151], v152, v[150:151]
	v_min_u32_e32 v150, 1, v150
	v_or_b32_e32 v150, v151, v150
	v_cvt_f32_u32_e32 v150, v150
	v_sub_u32_e32 v151, 32, v152
	s_cmp_gt_i32 s50, 15
	v_ldexp_f32 v152, v150, v151
	v_pk_fma_f32 v[150:151], v[152:153], s[40:41], v[166:167] op_sel_hi:[1,0,0]
	s_nop 0
	v_mul_f32_e32 v152, 0x4b800000, v151
	v_cmp_gt_f32_e64 s[36:37], s96, v151
	v_cmp_gt_f32_e32 vcc, s96, v150
	s_nop 0
	v_cndmask_b32_e64 v151, v151, v152, s[36:37]
	v_rsq_f32_e32 v151, v151
	s_nop 0
	v_mul_f32_e32 v152, 0x45800000, v151
	v_cndmask_b32_e64 v152, v151, v152, s[36:37]
	v_mul_f32_e32 v151, 0x4b800000, v150
	v_cndmask_b32_e32 v150, v150, v151, vcc
	v_rsq_f32_e32 v150, v150
	s_nop 0
	v_mul_f32_e32 v151, 0x45800000, v150
	v_cndmask_b32_e32 v150, v150, v151, vcc
	v_ffbh_u32_e32 v151, v149
	v_min_u32_e32 v151, 32, v151
	v_lshlrev_b64 v[148:149], v151, v[148:149]
	v_min_u32_e32 v148, 1, v148
	v_or_b32_e32 v148, v149, v148
	v_cvt_f32_u32_e32 v148, v148
	v_sub_u32_e32 v149, 32, v151
	v_ldexp_f32 v149, v148, v149
	v_ffbh_u32_e32 v148, v147
	v_min_u32_e32 v148, 32, v148
	v_lshlrev_b64 v[146:147], v148, v[146:147]
	v_min_u32_e32 v146, 1, v146
	v_or_b32_e32 v146, v147, v146
	v_cvt_f32_u32_e32 v146, v146
	v_sub_u32_e32 v147, 32, v148
	v_ldexp_f32 v148, v146, v147
	v_pk_fma_f32 v[146:147], v[148:149], s[40:41], v[166:167] op_sel_hi:[1,0,0]
	s_nop 0
	v_mul_f32_e32 v148, 0x4b800000, v147
	v_cmp_gt_f32_e64 s[36:37], s96, v147
	v_cmp_gt_f32_e32 vcc, s96, v146
	s_nop 0
	v_cndmask_b32_e64 v147, v147, v148, s[36:37]
	v_rsq_f32_e32 v147, v147
	s_nop 0
	v_mul_f32_e32 v148, 0x45800000, v147
	v_cndmask_b32_e64 v148, v147, v148, s[36:37]
	v_mul_f32_e32 v147, 0x4b800000, v146
	v_cndmask_b32_e32 v146, v146, v147, vcc
	v_rsq_f32_e32 v146, v146
	s_nop 0
	v_mul_f32_e32 v147, 0x45800000, v146
	v_cndmask_b32_e32 v146, v146, v147, vcc
	v_ffbh_u32_e32 v147, v145
	v_min_u32_e32 v147, 32, v147
	v_lshlrev_b64 v[144:145], v147, v[144:145]
	v_min_u32_e32 v144, 1, v144
	v_or_b32_e32 v144, v145, v144
	v_cvt_f32_u32_e32 v144, v144
	v_sub_u32_e32 v145, 32, v147
	v_ldexp_f32 v145, v144, v145
	v_ffbh_u32_e32 v144, v143
	v_min_u32_e32 v144, 32, v144
	v_lshlrev_b64 v[142:143], v144, v[142:143]
	v_min_u32_e32 v142, 1, v142
	v_or_b32_e32 v142, v143, v142
	v_cvt_f32_u32_e32 v142, v142
	v_sub_u32_e32 v143, 32, v144
	v_ldexp_f32 v144, v142, v143
	v_pk_fma_f32 v[142:143], v[144:145], s[40:41], v[166:167] op_sel_hi:[1,0,0]
	s_nop 0
	v_mul_f32_e32 v144, 0x4b800000, v143
	v_cmp_gt_f32_e64 s[36:37], s96, v143
	v_cmp_gt_f32_e32 vcc, s96, v142
	s_nop 0
	v_cndmask_b32_e64 v143, v143, v144, s[36:37]
	v_rsq_f32_e32 v143, v143
	s_nop 0
	v_mul_f32_e32 v144, 0x45800000, v143
	v_cndmask_b32_e64 v144, v143, v144, s[36:37]
	v_mul_f32_e32 v143, 0x4b800000, v142
	v_cndmask_b32_e32 v142, v142, v143, vcc
	v_rsq_f32_e32 v142, v142
	s_mov_b64 s[36:37], -1
	v_mul_f32_e32 v143, 0x45800000, v142
	v_cndmask_b32_e32 v142, v142, v143, vcc
	s_cbranch_scc0 .LBB0_2021
	s_cmp_gt_u32 s50, 19
	s_cbranch_scc0 .LBB0_2018
	s_and_b64 vcc, exec, s[38:39]
	s_cbranch_vccz .LBB0_2015
	v_readlane_b32 s36, v253, 45
	v_cmp_gt_u32_e32 vcc, 16, v159
	v_readlane_b32 s37, v253, 46
	s_and_b64 s[40:41], s[36:37], vcc
	s_and_saveexec_b64 s[36:37], s[40:41]
	s_cbranch_execz .LBB0_2014
	v_ashrrev_i32_e32 v159, 31, v158
	v_lshlrev_b64 v[166:167], 5, v[158:159]
	v_mul_f32_e32 v172, 0x3d3504f3, v156
	v_lshl_add_u64 v[170:171], s[42:43], 0, v[166:167]
	v_pk_mul_f32 v[168:169], v[172:173], v[128:129] op_sel_hi:[0,1]
	v_pk_mul_f32 v[166:167], v[172:173], v[126:127] op_sel_hi:[0,1]
	global_store_dwordx4 v[170:171], v[166:169], off sc1
	v_mul_f32_e32 v174, 0x3d3504f3, v154
	s_mov_b64 s[40:41], 0x1000
	v_pk_mul_f32 v[168:169], v[172:173], v[124:125] op_sel_hi:[0,1]
	v_pk_mul_f32 v[166:167], v[172:173], v[122:123] op_sel_hi:[0,1]
	global_store_dwordx4 v[170:171], v[166:169], off offset:16 sc1
	s_nop 1
	v_or_b32_e32 v166, 16, v158
	v_ashrrev_i32_e32 v167, 31, v166
	v_lshlrev_b64 v[166:167], 5, v[166:167]
	v_lshl_add_u64 v[172:173], s[42:43], 0, v[166:167]
	v_pk_mul_f32 v[168:169], v[174:175], v[116:117] op_sel_hi:[0,1]
	v_pk_mul_f32 v[166:167], v[174:175], v[114:115] op_sel_hi:[0,1]
	global_store_dwordx4 v[172:173], v[166:169], off sc1
	s_nop 1
	v_pk_mul_f32 v[168:169], v[174:175], v[108:109] op_sel_hi:[0,1]
	v_pk_mul_f32 v[166:167], v[174:175], v[106:107] op_sel_hi:[0,1]
	global_store_dwordx4 v[172:173], v[166:169], off offset:16 sc1
	v_mul_f32_e32 v174, 0x3d3504f3, v152
	s_nop 0
	v_or_b32_e32 v166, 32, v158
	v_ashrrev_i32_e32 v167, 31, v166
	v_lshlrev_b64 v[166:167], 5, v[166:167]
	v_lshl_add_u64 v[172:173], s[42:43], 0, v[166:167]
	v_pk_mul_f32 v[168:169], v[174:175], v[100:101] op_sel_hi:[0,1]
	v_pk_mul_f32 v[166:167], v[174:175], v[98:99] op_sel_hi:[0,1]
	global_store_dwordx4 v[172:173], v[166:169], off sc1
	s_nop 1
	v_pk_mul_f32 v[168:169], v[174:175], v[92:93] op_sel_hi:[0,1]
	v_pk_mul_f32 v[166:167], v[174:175], v[90:91] op_sel_hi:[0,1]
	global_store_dwordx4 v[172:173], v[166:169], off offset:16 sc1
	v_mul_f32_e32 v174, 0x3d3504f3, v150
	s_nop 0
	v_or_b32_e32 v166, 48, v158
	v_ashrrev_i32_e32 v167, 31, v166
	v_lshlrev_b64 v[166:167], 5, v[166:167]
	v_lshl_add_u64 v[172:173], s[42:43], 0, v[166:167]
	v_pk_mul_f32 v[168:169], v[174:175], v[84:85] op_sel_hi:[0,1]
	v_pk_mul_f32 v[166:167], v[174:175], v[82:83] op_sel_hi:[0,1]
	global_store_dwordx4 v[172:173], v[166:169], off sc1
	s_nop 1
	v_pk_mul_f32 v[168:169], v[174:175], v[76:77] op_sel_hi:[0,1]
	v_pk_mul_f32 v[166:167], v[174:175], v[74:75] op_sel_hi:[0,1]
	global_store_dwordx4 v[172:173], v[166:169], off offset:16 sc1
	v_lshl_add_u64 v[172:173], v[170:171], 0, s[40:41]
	s_movk_i32 s40, 0x1000
	v_mul_f32_e32 v174, 0x3d3504f3, v148
	v_add_co_u32_e32 v176, vcc, s40, v170
	v_pk_mul_f32 v[168:169], v[174:175], v[64:65] op_sel_hi:[0,1]
	v_pk_mul_f32 v[166:167], v[174:175], v[62:63] op_sel_hi:[0,1]
	v_addc_co_u32_e32 v177, vcc, 0, v171, vcc
	global_store_dwordx4 v[176:177], v[166:169], off sc1
	s_mov_b64 s[40:41], 0x1200
	s_nop 0
	v_pk_mul_f32 v[168:169], v[174:175], v[60:61] op_sel_hi:[0,1]
	v_pk_mul_f32 v[166:167], v[174:175], v[58:59] op_sel_hi:[0,1]
	v_mul_f32_e32 v174, 0x3d3504f3, v146
	global_store_dwordx4 v[172:173], v[166:169], off offset:16 sc1
	v_lshl_add_u64 v[172:173], v[170:171], 0, s[40:41]
	s_mov_b64 s[40:41], 0x1400
	v_pk_mul_f32 v[168:169], v[174:175], v[56:57] op_sel_hi:[0,1]
	v_pk_mul_f32 v[166:167], v[174:175], v[54:55] op_sel_hi:[0,1]
	global_store_dwordx4 v[176:177], v[166:169], off offset:512 sc1
	s_nop 1
	v_pk_mul_f32 v[168:169], v[174:175], v[48:49] op_sel_hi:[0,1]
	v_pk_mul_f32 v[166:167], v[174:175], v[46:47] op_sel_hi:[0,1]
	v_mul_f32_e32 v174, 0x3d3504f3, v144
	global_store_dwordx4 v[172:173], v[166:169], off offset:16 sc1
	v_lshl_add_u64 v[172:173], v[170:171], 0, s[40:41]
	s_mov_b64 s[40:41], 0x1600
	v_pk_mul_f32 v[168:169], v[174:175], v[40:41] op_sel_hi:[0,1]
	v_pk_mul_f32 v[166:167], v[174:175], v[38:39] op_sel_hi:[0,1]
	global_store_dwordx4 v[176:177], v[166:169], off offset:1024 sc1
	v_lshl_add_u64 v[170:171], v[170:171], 0, s[40:41]
	s_nop 0
	v_pk_mul_f32 v[168:169], v[174:175], v[32:33] op_sel_hi:[0,1]
	v_pk_mul_f32 v[166:167], v[174:175], v[30:31] op_sel_hi:[0,1]
	global_store_dwordx4 v[172:173], v[166:169], off offset:16 sc1
	v_mul_f32_e32 v172, 0x3d3504f3, v142
	s_nop 0
	v_pk_mul_f32 v[168:169], v[172:173], v[24:25] op_sel_hi:[0,1]
	v_pk_mul_f32 v[166:167], v[172:173], v[22:23] op_sel_hi:[0,1]
	global_store_dwordx4 v[176:177], v[166:169], off offset:1536 sc1
	s_nop 1
	v_pk_mul_f32 v[168:169], v[172:173], v[16:17] op_sel_hi:[0,1]
	v_pk_mul_f32 v[166:167], v[172:173], v[14:15] op_sel_hi:[0,1]
	global_store_dwordx4 v[170:171], v[166:169], off offset:16 sc1
